# speedup vs baseline: 1.0076x; 1.0076x over previous
_Z10agg_kernelPKjPKiPKDF16_S4_PKfS4_S0_S2_S2_S2_S2_Pf:
	s_and_b32 s3, s2, 1
	s_lshr_b32 s4, s2, 1
	s_load_dwordx16 s[8:23], s[0:1], 0x0
	s_load_dwordx8 s[24:31], s[0:1], 0x40
	s_mul_i32 s6, s4, 0xc4
	s_sub_u32 s5, 0xc350, s6
	s_min_u32 s5, s5, 0xc4
	v_lshrrev_b32_e32 v2, 2, v0
	v_and_b32_e32 v1, 3, v0
	v_lshrrev_b32_e32 v13, 1, v1
	v_lshl_add_u32 v13, s3, 1, v13
	v_lshlrev_b32_e32 v13, 2, v13
	v_lshlrev_b32_e32 v1, 4, v1
	s_lshl_b32 s52, s4, 2
	s_waitcnt lgkmcnt(0)
	s_add_u32 s52, s10, s52
	s_addc_u32 s53, s11, 0
	s_load_dwordx2 s[32:33], s[52:53], 0x0
	s_load_dwordx2 s[36:37], s[52:53], 0x404
	v_add_u32_e32 v40, s6, v2
	v_min_u32_e32 v40, 0xc34f, v40
	v_lshlrev_b32_e32 v40, 6, v40
	v_add3_u32 v40, v40, v13, 16
	global_load_dword v3, v40, s[16:17] nt
	global_load_dword v4, v40, s[16:17] offset:32 nt
	v_lshlrev_b32_e32 v62, 2, v0
	v_mov_b32_e32 v63, 0
	ds_write_b32 v62, v63 offset:24448
	v_cmp_gt_u32_e32 vcc, 0x200, v0
	s_and_saveexec_b64 s[60:61], vcc
	ds_write_b32 v62, v63 offset:28544
	s_mov_b64 exec, s[60:61]
	s_waitcnt lgkmcnt(0)
	s_sub_u32 s38, s33, s32
	s_sub_u32 s39, s37, s36
	s_lshl_b32 s52, s32, 2
	s_add_u32 s42, s8, s52
	s_addc_u32 s43, s9, 0
	s_add_u32 s52, s36, 0xc3500
	s_lshl_b32 s52, s52, 2
	s_add_u32 s44, s8, s52
	s_addc_u32 s45, s9, 0
	s_max_i32 s52, s38, 1
	s_sub_u32 s52, s52, 1
	s_max_i32 s53, s39, 1
	s_sub_u32 s53, s53, 1
	s_movk_i32 s46, 0x80
	s_movk_i32 s55, 0x62
	s_movk_i32 s47, 0x61a8
	v_min_u32_e32 v41, s52, v0
	v_lshlrev_b32_e32 v41, 2, v41
	global_load_dword v8, v41, s[42:43] nt
	v_min_u32_e32 v41, s53, v0
	v_lshlrev_b32_e32 v41, 2, v41
	global_load_dword v24, v41, s[44:45] nt
	v_add_u32_e32 v40, 0x400, v0
	v_min_u32_e32 v41, s52, v40
	v_lshlrev_b32_e32 v41, 2, v41
	global_load_dword v9, v41, s[42:43] nt
	v_min_u32_e32 v41, s53, v40
	v_lshlrev_b32_e32 v41, 2, v41
	global_load_dword v25, v41, s[44:45] nt
	v_add_u32_e32 v40, 0x800, v0
	v_min_u32_e32 v41, s52, v40
	v_lshlrev_b32_e32 v41, 2, v41
	global_load_dword v10, v41, s[42:43] nt
	v_min_u32_e32 v41, s53, v40
	v_lshlrev_b32_e32 v41, 2, v41
	global_load_dword v26, v41, s[44:45] nt
	v_add_u32_e32 v40, 0xc00, v0
	v_min_u32_e32 v41, s52, v40
	v_lshlrev_b32_e32 v41, 2, v41
	global_load_dword v11, v41, s[42:43] nt
	v_min_u32_e32 v41, s53, v40
	v_lshlrev_b32_e32 v41, 2, v41
	global_load_dword v27, v41, s[44:45] nt
	v_mov_b32_e32 v61, 1
	v_mov_b32_e32 v43, 0xc4
	s_barrier
	s_waitcnt vmcnt(7)
	v_bfe_u32 v28, v8, 16, 7
	v_bfe_u32 v42, v8, 23, 1
	v_and_b32_e32 v44, 0xffff, v8
	v_mad_u32_u24 v28, v42, s55, v28
	v_cmp_le_u32_e32 vcc, s47, v44
	v_lshlrev_b32_e32 v28, 2, v28
	s_nop 0
	v_cndmask_b32_e32 v42, 0, v43, vcc
	v_lshl_add_u32 v28, v42, 2, v28
	v_cmp_gt_u32_e32 vcc, s38, v0
	s_and_saveexec_b64 s[60:61], vcc
	ds_add_rtn_u32 v16, v28, v61 offset:24448
	s_mov_b64 exec, s[60:61]
	s_waitcnt vmcnt(6)
	v_bfe_u32 v32, v24, 16, 7
	v_bfe_u32 v42, v24, 23, 1
	v_and_b32_e32 v44, 0xffff, v24
	v_mad_u32_u24 v32, v42, s55, v32
	v_cmp_le_u32_e32 vcc, s47, v44
	v_lshlrev_b32_e32 v32, 2, v32
	s_nop 0
	v_cndmask_b32_e32 v42, 0, v43, vcc
	v_lshl_add_u32 v32, v42, 2, v32
	v_cmp_gt_u32_e32 vcc, s39, v0
	s_and_saveexec_b64 s[60:61], vcc
	ds_add_rtn_u32 v20, v32, v61 offset:26496
	s_mov_b64 exec, s[60:61]
	s_waitcnt vmcnt(5)
	v_add_u32_e32 v40, 0x400, v0
	v_bfe_u32 v29, v9, 16, 7
	v_bfe_u32 v42, v9, 23, 1
	v_and_b32_e32 v44, 0xffff, v9
	v_mad_u32_u24 v29, v42, s55, v29
	v_cmp_le_u32_e32 vcc, s47, v44
	v_lshlrev_b32_e32 v29, 2, v29
	s_nop 0
	v_cndmask_b32_e32 v42, 0, v43, vcc
	v_lshl_add_u32 v29, v42, 2, v29
	v_cmp_gt_u32_e32 vcc, s38, v40
	s_and_saveexec_b64 s[60:61], vcc
	ds_add_rtn_u32 v17, v29, v61 offset:24448
	s_mov_b64 exec, s[60:61]
	s_waitcnt vmcnt(4)
	v_bfe_u32 v33, v25, 16, 7
	v_bfe_u32 v42, v25, 23, 1
	v_and_b32_e32 v44, 0xffff, v25
	v_mad_u32_u24 v33, v42, s55, v33
	v_cmp_le_u32_e32 vcc, s47, v44
	v_lshlrev_b32_e32 v33, 2, v33
	s_nop 0
	v_cndmask_b32_e32 v42, 0, v43, vcc
	v_lshl_add_u32 v33, v42, 2, v33
	v_cmp_gt_u32_e32 vcc, s39, v40
	s_and_saveexec_b64 s[60:61], vcc
	ds_add_rtn_u32 v21, v33, v61 offset:26496
	s_mov_b64 exec, s[60:61]
	s_waitcnt vmcnt(3)
	v_add_u32_e32 v40, 0x800, v0
	v_bfe_u32 v30, v10, 16, 7
	v_bfe_u32 v42, v10, 23, 1
	v_and_b32_e32 v44, 0xffff, v10
	v_mad_u32_u24 v30, v42, s55, v30
	v_cmp_le_u32_e32 vcc, s47, v44
	v_lshlrev_b32_e32 v30, 2, v30
	s_nop 0
	v_cndmask_b32_e32 v42, 0, v43, vcc
	v_lshl_add_u32 v30, v42, 2, v30
	v_cmp_gt_u32_e32 vcc, s38, v40
	s_and_saveexec_b64 s[60:61], vcc
	ds_add_rtn_u32 v18, v30, v61 offset:24448
	s_mov_b64 exec, s[60:61]
	s_waitcnt vmcnt(2)
	v_bfe_u32 v34, v26, 16, 7
	v_bfe_u32 v42, v26, 23, 1
	v_and_b32_e32 v44, 0xffff, v26
	v_mad_u32_u24 v34, v42, s55, v34
	v_cmp_le_u32_e32 vcc, s47, v44
	v_lshlrev_b32_e32 v34, 2, v34
	s_nop 0
	v_cndmask_b32_e32 v42, 0, v43, vcc
	v_lshl_add_u32 v34, v42, 2, v34
	v_cmp_gt_u32_e32 vcc, s39, v40
	s_and_saveexec_b64 s[60:61], vcc
	ds_add_rtn_u32 v22, v34, v61 offset:26496
	s_mov_b64 exec, s[60:61]
	s_waitcnt vmcnt(1)
	v_add_u32_e32 v40, 0xc00, v0
	v_bfe_u32 v31, v11, 16, 7
	v_bfe_u32 v42, v11, 23, 1
	v_and_b32_e32 v44, 0xffff, v11
	v_mad_u32_u24 v31, v42, s55, v31
	v_cmp_le_u32_e32 vcc, s47, v44
	v_lshlrev_b32_e32 v31, 2, v31
	s_nop 0
	v_cndmask_b32_e32 v42, 0, v43, vcc
	v_lshl_add_u32 v31, v42, 2, v31
	v_cmp_gt_u32_e32 vcc, s38, v40
	s_and_saveexec_b64 s[60:61], vcc
	ds_add_rtn_u32 v19, v31, v61 offset:24448
	s_mov_b64 exec, s[60:61]
	s_waitcnt vmcnt(0)
	v_bfe_u32 v35, v27, 16, 7
	v_bfe_u32 v42, v27, 23, 1
	v_and_b32_e32 v44, 0xffff, v27
	v_mad_u32_u24 v35, v42, s55, v35
	v_cmp_le_u32_e32 vcc, s47, v44
	v_lshlrev_b32_e32 v35, 2, v35
	s_nop 0
	v_cndmask_b32_e32 v42, 0, v43, vcc
	v_lshl_add_u32 v35, v42, 2, v35
	v_cmp_gt_u32_e32 vcc, s39, v40
	s_and_saveexec_b64 s[60:61], vcc
	ds_add_rtn_u32 v23, v35, v61 offset:26496
	s_mov_b64 exec, s[60:61]
	s_waitcnt lgkmcnt(0)
	s_barrier
	ds_read_b32 v40, v62 offset:24448
	v_and_b32_e32 v44, 63, v0
	v_lshrrev_b32_e32 v45, 6, v0
	v_lshlrev_b32_e32 v45, 2, v45
	v_and_b32_e32 v52, 0x1ff, v0
	v_lshrrev_b32_e32 v51, 9, v0
	v_cmp_le_u32_e32 vcc, 0xc4, v52
	v_mov_b32_e32 v47, 31
	s_nop 0
	v_cndmask_b32_e64 v53, 0, 1, vcc
	v_mul_u32_u24_e32 v54, 0xc4, v53
	v_sub_u32_e32 v54, v52, v54
	v_lshl_add_u32 v53, v51, 1, v53
	s_waitcnt lgkmcnt(0)
	v_min_u32_e32 v55, 31, v40
	v_sub_u32_e32 v55, v47, v55
	v_and_b32_e32 v47, 3, v0
	v_lshl_or_b32 v55, v55, 2, v47
	v_lshl_add_u32 v55, v53, 7, v55
	v_lshlrev_b32_e32 v55, 2, v55
	v_cmp_gt_u32_e32 vcc, 0x188, v52
	s_and_saveexec_b64 s[60:61], vcc
	ds_add_rtn_u32 v51, v55, v61 offset:28544
	s_mov_b64 exec, s[60:61]
	v_mov_b32_e32 v41, v40
	s_nop 1
	v_add_u32_dpp v41, v41, v41 row_shr:1 row_mask:0xf bank_mask:0xf
	s_nop 1
	v_add_u32_dpp v41, v41, v41 row_shr:2 row_mask:0xf bank_mask:0xf
	s_nop 1
	v_add_u32_dpp v41, v41, v41 row_shr:4 row_mask:0xf bank_mask:0xf
	s_nop 1
	v_add_u32_dpp v41, v41, v41 row_shr:8 row_mask:0xf bank_mask:0xf
	s_nop 1
	v_add_u32_dpp v41, v41, v41 row_bcast:15 row_mask:0xa bank_mask:0xf
	s_nop 1
	v_add_u32_dpp v41, v41, v41 row_bcast:31 row_mask:0xc bank_mask:0xf
	v_cmp_eq_u32_e32 vcc, 63, v44
	s_and_saveexec_b64 s[60:61], vcc
	ds_write_b32 v45, v41 offset:21056
	s_mov_b64 exec, s[60:61]
	s_waitcnt lgkmcnt(0)
	s_barrier
	v_cmp_gt_u32_e32 vcc, 0x200, v0
	s_and_saveexec_b64 s[60:61], vcc
	s_cbranch_execz .Lagg_bins_done
	ds_read_b32 v48, v62 offset:28544
	s_waitcnt lgkmcnt(0)
	v_mov_b32_e32 v49, v48
	s_nop 1
	v_add_u32_dpp v49, v49, v49 row_shr:1 row_mask:0xf bank_mask:0xf
	s_nop 1
	v_add_u32_dpp v49, v49, v49 row_shr:2 row_mask:0xf bank_mask:0xf
	s_nop 1
	v_add_u32_dpp v49, v49, v49 row_shr:4 row_mask:0xf bank_mask:0xf
	s_nop 1
	v_add_u32_dpp v49, v49, v49 row_shr:8 row_mask:0xf bank_mask:0xf
	s_nop 1
	v_add_u32_dpp v49, v49, v49 row_bcast:15 row_mask:0xa bank_mask:0xf
	s_nop 1
	v_add_u32_dpp v49, v49, v49 row_bcast:31 row_mask:0xc bank_mask:0xf
	s_nop 0
	v_sub_u32_e32 v50, v49, v48
	ds_write_b32 v62, v50 offset:32640
	v_cmp_eq_u32_e32 vcc, 63, v44
	s_and_b64 exec, exec, vcc
	ds_write_b32 v45, v49 offset:36736

.Lagg_scatter_done:
	v_and_b32_e32 v40, 1, v0
	v_cmp_eq_u32_e32 vcc, 0, v40
	s_movk_i32 s52, 0xc4
	v_cmp_gt_u32_e64 s[60:61], s52, v2
	s_and_b64 vcc, vcc, s[60:61]
	s_and_saveexec_b64 s[60:61], vcc
	v_bfe_u32 v40, v0, 1, 1
	v_mul_u32_u24_e32 v40, 0x310, v40
	v_lshl_add_u32 v40, v2, 2, v40
	ds_write_b32 v40, v3 offset:21248
	ds_write_b32 v40, v4 offset:22816
	s_mov_b64 exec, s[60:61]
	s_lshl_b32 s52, s3, 7
	s_add_u32 s52, s18, s52
	s_addc_u32 s53, s19, 0
	v_lshlrev_b32_e32 v40, 1, v1
	global_load_dwordx4 v[16:19], v40, s[52:53]
	global_load_dwordx4 v[20:23], v40, s[52:53] offset:16
	global_load_dword v56, v13, s[20:21] offset:0
	global_load_dword v57, v13, s[20:21] offset:16
	s_waitcnt lgkmcnt(0)
	s_barrier
	v_lshrrev_b32_e32 v40, 6, v0
	s_nop 0
	v_readfirstlane_b32 s41, v40
	s_cmp_gt_u32 s41, 13
	s_cbranch_scc1 .Lagg_exit
	v_mov_b32_e32 v15, 1.0
	s_lshl_b32 s52, s3, 8
	s_add_u32 s68, s30, s52
	s_addc_u32 s69, s31, 0
	s_mul_i32 s52, s3, 0x61a800
	s_add_u32 s70, s14, s52
	s_addc_u32 s71, s15, 0
	s_mul_i32 s52, s3, 0x61a800
	s_add_u32 s48, s12, s52
	s_addc_u32 s49, s13, 0
	s_waitcnt vmcnt(0)
	v_not_b32_e32 v58, v56
	v_and_b32_e32 v59, 0x7fffffff, v56
	v_cmp_gt_i32_e32 vcc, 0, v56
	s_nop 1
	v_cndmask_b32_e32 v56, v58, v59, vcc
	v_not_b32_e32 v58, v57
	v_and_b32_e32 v59, 0x7fffffff, v57
	v_cmp_gt_i32_e32 vcc, 0, v57
	s_nop 1
	v_cndmask_b32_e32 v57, v58, v59, vcc
	v_mov_b32_e32 v46, v56
	v_add_f32_e32 v14, v56, v57
	v_mul_f32_e32 v58, 0x3c23d70a, v14
	v_max_f32_e32 v14, v14, v58
	s_cmp_eq_u32 s7, 0
	s_cbranch_scc1 .Lagg_slow_0
	s_lshl_b32 s40, s41, 4
	s_cmp_eq_u32 s40, 0xc0
	s_cselect_b32 s40, 0xd0, s40
	s_cmp_eq_u32 s41, 13
	s_cselect_b32 s40, 0xc0, s40
	v_bfe_u32 v63, v0, 2, 4
	v_add_u32_e32 v63, s40, v63
	v_cmp_gt_u32_e32 vcc, 0xc4, v63
	s_and_saveexec_b64 s[58:59], vcc
	s_cbranch_execz .Lagg_phasedone_0_0
	v_lshlrev_b32_e32 v63, 1, v63
	ds_read_u16 v60, v63 offset:18432
	v_lshrrev_b32_e32 v63, 2, v1
	s_waitcnt lgkmcnt(0)
	v_lshlrev_b32_e32 v61, 2, v60
	ds_read_b32 v58, v61 offset:14336
	ds_read_b32 v59, v61 offset:14340
	v_bfe_u32 v57, v0, 1, 1
	v_mul_u32_u24_e32 v57, 0x310, v57
	v_lshl_add_u32 v57, v60, 2, v57
	ds_read_b32 v57, v57 offset:21248
	v_lshl_add_u32 v61, v60, 4, v63
	v_mov_b32_e32 v45, 0
	v_mov_b32_e32 v48, 0
	v_mov_b32_e32 v49, 0
	v_mov_b32_e32 v50, 0
	v_mov_b32_e32 v51, 0
	v_mov_b32_e32 v52, 0
	v_mov_b32_e32 v53, 0
	v_mov_b32_e32 v54, 0
	v_mov_b32_e32 v55, 0
	s_waitcnt lgkmcnt(0)
	v_lshlrev_b32_e32 v41, 1, v58
	v_lshlrev_b32_e32 v42, 1, v59
	v_cmp_lt_u32_e32 vcc, v41, v42
	s_and_saveexec_b64 s[64:65], vcc
	s_cbranch_execz .Lagg_listdone_0_0
	ds_read_u16 v40, v41
	v_add_u32_e32 v41, 2, v41
	s_waitcnt lgkmcnt(0)
	v_mad_u32_u16 v24, v40, s46, v1
	global_load_dwordx4 v[28:31], v24, s[48:49] offset:64
	global_load_dwordx4 v[24:27], v24, s[48:49]
	s_waitcnt lgkmcnt(0)
	v_add_f32_e32 v47, v46, v57
	v_mul_f32_e32 v56, 0x3c23d70a, v47
	v_max_f32_e32 v47, v47, v56
	v_sub_f32_e32 v43, v57, v47
	v_mul_f32_e32 v43, 0.5, v43
	v_mul_f32_e32 v44, 0xbf7d70a4, v47

.Lagg_join_0:
	s_waitcnt vmcnt(0) lgkmcnt(0)
	s_barrier
	s_lshl_b32 s52, s3, 7
	s_add_u32 s52, s52, 0x100
	s_add_u32 s52, s18, s52
	s_addc_u32 s53, s19, 0
	v_lshlrev_b32_e32 v40, 1, v1
	global_load_dwordx4 v[16:19], v40, s[52:53]
	global_load_dwordx4 v[20:23], v40, s[52:53] offset:16
	global_load_dword v43, v13, s[20:21] offset:32
	global_load_dword v44, v13, s[20:21] offset:48
	v_cmp_gt_u32_e32 vcc, s5, v2
	s_and_saveexec_b64 s[58:59], vcc
	v_lshlrev_b32_e32 v61, 2, v0
	v_add_u32_e32 v60, 0x6e40, v61
	ds_read_b32 v48, v61 offset:24448
	ds_read_b32 v49, v61 offset:27584
	ds_read_b32 v50, v61 offset:30720
	ds_read_b32 v51, v61 offset:33856
	ds_read_b32 v52, v61 offset:36992
	ds_read_b32 v53, v61 offset:40128
	ds_read_b32 v54, v61 offset:43264
	ds_read_b32 v55, v61 offset:46400
	ds_read_b32 v45, v61 offset:49536
	s_waitcnt lgkmcnt(0)
	ds_read_b32 v24, v60 offset:24448
	ds_read_b32 v25, v60 offset:27584
	ds_read_b32 v26, v60 offset:30720
	ds_read_b32 v27, v60 offset:33856
	ds_read_b32 v28, v60 offset:36992
	ds_read_b32 v29, v60 offset:40128
	ds_read_b32 v30, v60 offset:43264
	ds_read_b32 v31, v60 offset:46400
	ds_read_b32 v32, v60 offset:49536
	v_mov_b32_e32 v62, 0x3c003c00
	s_waitcnt lgkmcnt(0)
	s_barrier
	v_pk_fma_f16 v48, v24, v62, v48
	v_pk_fma_f16 v49, v25, v62, v49
	v_pk_fma_f16 v50, v26, v62, v50
	v_pk_fma_f16 v51, v27, v62, v51
	v_pk_fma_f16 v52, v28, v62, v52
	v_pk_fma_f16 v53, v29, v62, v53
	v_pk_fma_f16 v54, v30, v62, v54
	v_pk_fma_f16 v55, v31, v62, v55
	v_add_f32_e32 v45, v45, v32
	s_cbranch_execz .Lagg_end_0
	v_add_f32_e32 v47, v46, v3
	v_mul_f32_e32 v58, 0x3c23d70a, v47
	v_max_f32_e32 v47, v47, v58
	v_sub_f32_e32 v58, v14, v47
	v_exp_f32_e32 v58, v58
	v_mul_f32_e32 v59, 0x33000000, v45
	v_rcp_f32_e32 v42, v45
	v_mul_f32_e32 v58, 0x24e69595, v58
	v_fma_f32 v60, -v45, v42, 1.0
	v_cmp_ge_f32_e64 s[62:63], v59, v58
	v_cmp_eq_f32_e32 vcc, 0, v45
	v_fmac_f32_e32 v42, v60, v42
	s_nop 1
	v_cndmask_b32_e64 v42, v42, 0, vcc
	s_or_b64 s[62:63], s[62:63], vcc
	s_mov_b64 s[66:67], exec
	s_andn2_b64 exec, exec, s[62:63]
	s_cbranch_execnz .Lagg_gmax_0

.Lagg_end_0:
	s_mov_b64 exec, s[58:59]
	s_mul_i32 s52, s3, 0x61a800
	s_add_u32 s52, s52, 0xc35000
	s_add_u32 s48, s12, s52
	s_addc_u32 s49, s13, 0
	s_waitcnt vmcnt(0)
	v_mov_b32_e32 v56, v43
	v_mov_b32_e32 v57, v44
	v_not_b32_e32 v58, v56
	v_and_b32_e32 v59, 0x7fffffff, v56
	v_cmp_gt_i32_e32 vcc, 0, v56
	s_nop 1
	v_cndmask_b32_e32 v56, v58, v59, vcc
	v_not_b32_e32 v58, v57
	v_and_b32_e32 v59, 0x7fffffff, v57
	v_cmp_gt_i32_e32 vcc, 0, v57
	s_nop 1
	v_cndmask_b32_e32 v57, v58, v59, vcc
	v_mov_b32_e32 v46, v56
	v_add_f32_e32 v14, v56, v57
	v_mul_f32_e32 v58, 0x3c23d70a, v14
	v_max_f32_e32 v14, v14, v58
	s_cmp_eq_u32 s7, 0
	s_cbranch_scc1 .Lagg_slow_1
	s_sub_u32 s40, 12, s41
	s_lshl_b32 s40, s40, 4
	s_cmp_eq_u32 s40, 0xc0
	s_cselect_b32 s40, 0xd0, s40
	s_cmp_eq_u32 s41, 13
	s_cselect_b32 s40, 0xc0, s40
	v_bfe_u32 v63, v0, 2, 4
	v_add_u32_e32 v63, s40, v63
	v_cmp_gt_u32_e32 vcc, 0xc4, v63
	s_and_saveexec_b64 s[58:59], vcc
	s_cbranch_execz .Lagg_phasedone_1_0
	v_lshlrev_b32_e32 v63, 1, v63
	ds_read_u16 v60, v63 offset:19216
	v_lshrrev_b32_e32 v63, 2, v1
	s_waitcnt lgkmcnt(0)
	v_lshlrev_b32_e32 v61, 2, v60
	ds_read_b32 v58, v61 offset:16384
	ds_read_b32 v59, v61 offset:16388
	v_bfe_u32 v57, v0, 1, 1
	v_mul_u32_u24_e32 v57, 0x310, v57
	v_lshl_add_u32 v57, v60, 2, v57
	ds_read_b32 v57, v57 offset:22816
	v_lshl_add_u32 v61, v60, 4, v63
	v_mov_b32_e32 v45, 0
	v_mov_b32_e32 v48, 0
	v_mov_b32_e32 v49, 0
	v_mov_b32_e32 v50, 0
	v_mov_b32_e32 v51, 0
	v_mov_b32_e32 v52, 0
	v_mov_b32_e32 v53, 0
	v_mov_b32_e32 v54, 0
	v_mov_b32_e32 v55, 0
	s_waitcnt lgkmcnt(0)
	v_lshlrev_b32_e32 v41, 1, v58
	v_lshlrev_b32_e32 v42, 1, v59
	v_add_u32_e32 v41, 0x1c00, v41
	v_add_u32_e32 v42, 0x1c00, v42
	v_cmp_lt_u32_e32 vcc, v41, v42
	s_and_saveexec_b64 s[64:65], vcc
	s_cbranch_execz .Lagg_listdone_1_0
	ds_read_u16 v40, v41
	v_add_u32_e32 v41, 2, v41
	s_waitcnt lgkmcnt(0)
	v_mad_u32_u16 v24, v40, s46, v1
	global_load_dwordx4 v[28:31], v24, s[48:49] offset:64
	global_load_dwordx4 v[24:27], v24, s[48:49]
	s_waitcnt lgkmcnt(0)
	v_add_f32_e32 v47, v46, v57
	v_mul_f32_e32 v56, 0x3c23d70a, v47
	v_max_f32_e32 v47, v47, v56
	v_sub_f32_e32 v43, v57, v47
	v_mul_f32_e32 v43, 0.5, v43
	v_mul_f32_e32 v44, 0xbf7d70a4, v47

.Lagg_join_1:
	v_cmp_gt_u32_e32 vcc, s5, v2
	s_and_saveexec_b64 s[58:59], vcc
	v_add_u32_e32 v61, s6, v2
	v_mad_u32_u24 v40, v61, s46, v1
	global_load_dwordx4 v[24:27], v40, s[70:71] nt
	global_load_dwordx4 v[28:31], v40, s[70:71] offset:64 nt
	v_lshlrev_b32_e32 v41, 9, v61
	v_lshl_add_u32 v41, v1, 2, v41
	s_mov_b64 exec, s[58:59]
	s_waitcnt lgkmcnt(0)
	s_barrier
	v_cmp_gt_u32_e32 vcc, s5, v2
	s_and_saveexec_b64 s[58:59], vcc
	v_lshlrev_b32_e32 v61, 2, v0
	v_add_u32_e32 v60, 0x6e40, v61
	ds_read_b32 v48, v61 offset:24448
	ds_read_b32 v49, v61 offset:27584
	ds_read_b32 v50, v61 offset:30720
	ds_read_b32 v51, v61 offset:33856
	ds_read_b32 v52, v61 offset:36992
	ds_read_b32 v53, v61 offset:40128
	ds_read_b32 v54, v61 offset:43264
	ds_read_b32 v55, v61 offset:46400
	ds_read_b32 v45, v61 offset:49536
	s_waitcnt lgkmcnt(0)
	ds_read_b32 v32, v60 offset:24448
	ds_read_b32 v33, v60 offset:27584
	ds_read_b32 v34, v60 offset:30720
	ds_read_b32 v35, v60 offset:33856
	ds_read_b32 v36, v60 offset:36992
	ds_read_b32 v37, v60 offset:40128
	ds_read_b32 v38, v60 offset:43264
	ds_read_b32 v39, v60 offset:46400
	ds_read_b32 v56, v60 offset:49536
	v_mov_b32_e32 v62, 0x3c003c00
	s_waitcnt lgkmcnt(0)
	v_pk_fma_f16 v48, v32, v62, v48
	v_pk_fma_f16 v49, v33, v62, v49
	v_pk_fma_f16 v50, v34, v62, v50
	v_pk_fma_f16 v51, v35, v62, v51
	v_pk_fma_f16 v52, v36, v62, v52
	v_pk_fma_f16 v53, v37, v62, v53
	v_pk_fma_f16 v54, v38, v62, v54
	v_pk_fma_f16 v55, v39, v62, v55
	v_add_f32_e32 v45, v45, v56
	s_cbranch_execz .Lagg_end_1
	v_add_f32_e32 v47, v46, v4
	v_mul_f32_e32 v58, 0x3c23d70a, v47
	v_max_f32_e32 v47, v47, v58
	v_sub_f32_e32 v58, v14, v47
	v_exp_f32_e32 v58, v58
	v_mul_f32_e32 v59, 0x33000000, v45
	v_rcp_f32_e32 v42, v45
	v_mul_f32_e32 v58, 0x24e69595, v58
	v_fma_f32 v60, -v45, v42, 1.0
	v_cmp_ge_f32_e64 s[62:63], v59, v58
	v_cmp_eq_f32_e32 vcc, 0, v45
	v_fmac_f32_e32 v42, v60, v42
	s_nop 1
	v_cndmask_b32_e64 v42, v42, 0, vcc
	s_or_b64 s[62:63], s[62:63], vcc
	s_mov_b64 s[66:67], exec
	s_andn2_b64 exec, exec, s[62:63]
	s_cbranch_execnz .Lagg_gmax_1
